# v027 + P4 residual epilogue rewritten as 4-deep load pipeline with counted vmcnt
# speedup vs baseline: 1.0036x; 1.0036x over previous
.LBB0_352:
	v_lshl_add_u32 v168, s16, 8, v1
	s_ashr_i32 s9, s16, 3
	v_ashrrev_i32_e32 v169, 31, v168
	v_lshl_or_b32 v160, s17, 8, v188
	s_mul_hi_i32 s11, s9, 0x6000
	s_mulk_i32 s9, 0x6000
	v_lshlrev_b64 v[162:163], 10, v[168:169]
	s_add_u32 s16, s36, s9
	v_ashrrev_i32_e32 v161, 31, v160
	v_readlane_b32 s72, v252, 13
	s_addc_u32 s17, s37, s11
	v_lshl_add_u64 v[232:233], v[162:163], 0, v[160:161]
	v_readlane_b32 s73, v252, 14
	v_lshl_add_u64 v[164:165], v[160:161], 2, s[16:17]
	global_load_dwordx4 v[122:125], v[164:165], off offset:16
	global_load_dwordx4 v[126:129], v[164:165], off
	global_load_dwordx4 v[190:193], v[164:165], off offset:528
	global_load_dwordx4 v[194:197], v[164:165], off offset:512
	v_readlane_b32 s18, v253, 2
	v_readlane_b32 s19, v253, 3
	s_andn2_b64 vcc, exec, s[2:3]
	s_mov_b64 s[16:17], 0x4000
	v_lshl_add_u64 v[234:235], v[232:233], 0, s[16:17]
	v_lshl_add_u64 v[248:249], v[232:233], 2, s[72:73]
	global_load_dwordx4 v[200:203], v[248:249], off offset:16
	global_load_dwordx4 v[204:207], v[248:249], off
	s_mov_b64 s[16:17], 0x8000
	v_lshl_add_u64 v[236:237], v[232:233], 0, s[16:17]
	v_lshl_add_u64 v[250:251], v[234:235], 2, s[72:73]
	global_load_dwordx4 v[208:211], v[250:251], off offset:16
	global_load_dwordx4 v[212:215], v[250:251], off
	s_mov_b64 s[16:17], 0xc000
	v_lshl_add_u64 v[238:239], v[232:233], 0, s[16:17]
	v_lshl_add_u64 v[248:249], v[236:237], 2, s[72:73]
	global_load_dwordx4 v[216:219], v[248:249], off offset:16
	global_load_dwordx4 v[220:223], v[248:249], off
	s_mov_b64 s[16:17], 0x20000
	v_lshl_add_u64 v[240:241], v[232:233], 0, s[16:17]
	s_mov_b64 s[16:17], 0x24000
	v_lshl_add_u64 v[242:243], v[232:233], 0, s[16:17]
	s_mov_b64 s[16:17], 0x28000
	v_lshl_add_u64 v[244:245], v[232:233], 0, s[16:17]
	s_mov_b64 s[16:17], 0x2c000
	v_lshl_add_u64 v[246:247], v[232:233], 0, s[16:17]
	v_lshl_add_u64 v[250:251], v[238:239], 2, s[72:73]
	global_load_dwordx4 v[224:227], v[250:251], off offset:16
	global_load_dwordx4 v[228:231], v[250:251], off
	s_mov_b64 s[16:17], -1
	v_readlane_b32 s74, v252, 15
	v_readlane_b32 s75, v252, 16
	v_readlane_b32 s76, v252, 17
	v_readlane_b32 s77, v252, 18
	v_readlane_b32 s78, v252, 19
	v_readlane_b32 s79, v252, 20
	v_readlane_b32 s80, v252, 21
	v_readlane_b32 s81, v252, 22
	v_readlane_b32 s82, v252, 23
	v_readlane_b32 s83, v252, 24
	v_readlane_b32 s84, v252, 25
	v_readlane_b32 s85, v252, 26
	v_readlane_b32 s86, v252, 27
	v_readlane_b32 s87, v252, 28
	s_waitcnt vmcnt(6)
	v_pk_fma_f32 v[202:203], v[132:133], v[124:125], v[202:203]
	v_pk_fma_f32 v[136:137], v[136:137], v[128:129], v[206:207]
	v_pk_fma_f32 v[134:135], v[134:135], v[126:127], v[204:205]
	v_pk_fma_f32 v[132:133], v[130:131], v[122:123], v[200:201]
	v_cvt_pk_bf16_f32 v130, v134, v135
	v_cvt_pk_bf16_f32 v131, v136, v137
	v_cvt_pk_bf16_f32 v132, v132, v133
	v_cvt_pk_bf16_f32 v133, v202, v203
	v_lshl_add_u64 v[198:199], v[232:233], 1, s[18:19]
	global_store_dwordx4 v[198:199], v[130:133], off
	v_lshl_add_u64 v[248:249], v[240:241], 2, s[72:73]
	global_load_dwordx4 v[200:203], v[248:249], off offset:16
	global_load_dwordx4 v[204:207], v[248:249], off
	s_waitcnt vmcnt(7)
	v_pk_fma_f32 v[210:211], v[116:117], v[124:125], v[210:211]
	v_pk_fma_f32 v[120:121], v[120:121], v[128:129], v[214:215]
	v_pk_fma_f32 v[118:119], v[118:119], v[126:127], v[212:213]
	v_pk_fma_f32 v[116:117], v[114:115], v[122:123], v[208:209]
	v_cvt_pk_bf16_f32 v114, v118, v119
	v_cvt_pk_bf16_f32 v115, v120, v121
	v_cvt_pk_bf16_f32 v116, v116, v117
	v_cvt_pk_bf16_f32 v117, v210, v211
	v_lshl_add_u64 v[166:167], v[234:235], 1, s[18:19]
	global_store_dwordx4 v[166:167], v[114:117], off
	v_lshl_add_u64 v[250:251], v[242:243], 2, s[72:73]
	global_load_dwordx4 v[208:211], v[250:251], off offset:16
	global_load_dwordx4 v[212:215], v[250:251], off
	s_waitcnt vmcnt(8)
	v_pk_fma_f32 v[218:219], v[108:109], v[124:125], v[218:219]
	v_pk_fma_f32 v[112:113], v[112:113], v[128:129], v[222:223]
	v_pk_fma_f32 v[110:111], v[110:111], v[126:127], v[220:221]
	v_pk_fma_f32 v[108:109], v[106:107], v[122:123], v[216:217]
	v_cvt_pk_bf16_f32 v106, v110, v111
	v_cvt_pk_bf16_f32 v107, v112, v113
	v_cvt_pk_bf16_f32 v108, v108, v109
	v_cvt_pk_bf16_f32 v109, v218, v219
	v_lshl_add_u64 v[198:199], v[236:237], 1, s[18:19]
	global_store_dwordx4 v[198:199], v[106:109], off
	v_lshl_add_u64 v[248:249], v[244:245], 2, s[72:73]
	global_load_dwordx4 v[216:219], v[248:249], off offset:16
	global_load_dwordx4 v[220:223], v[248:249], off
	s_waitcnt vmcnt(9)
	v_pk_fma_f32 v[226:227], v[100:101], v[124:125], v[226:227]
	v_pk_fma_f32 v[104:105], v[104:105], v[128:129], v[230:231]
	v_pk_fma_f32 v[102:103], v[102:103], v[126:127], v[228:229]
	v_pk_fma_f32 v[100:101], v[98:99], v[122:123], v[224:225]
	v_cvt_pk_bf16_f32 v98, v102, v103
	v_cvt_pk_bf16_f32 v99, v104, v105
	v_cvt_pk_bf16_f32 v100, v100, v101
	v_cvt_pk_bf16_f32 v101, v226, v227
	v_lshl_add_u64 v[166:167], v[238:239], 1, s[18:19]
	global_store_dwordx4 v[166:167], v[98:101], off
	v_lshl_add_u64 v[250:251], v[246:247], 2, s[72:73]
	global_load_dwordx4 v[224:227], v[250:251], off offset:16
	global_load_dwordx4 v[228:231], v[250:251], off
	s_waitcnt vmcnt(9)
	v_pk_fma_f32 v[202:203], v[92:93], v[124:125], v[202:203]
	v_pk_fma_f32 v[96:97], v[96:97], v[128:129], v[206:207]
	v_pk_fma_f32 v[94:95], v[94:95], v[126:127], v[204:205]
	v_pk_fma_f32 v[92:93], v[90:91], v[122:123], v[200:201]
	v_cvt_pk_bf16_f32 v90, v94, v95
	v_cvt_pk_bf16_f32 v91, v96, v97
	v_cvt_pk_bf16_f32 v92, v92, v93
	v_cvt_pk_bf16_f32 v93, v202, v203
	v_lshl_add_u64 v[198:199], v[240:241], 1, s[18:19]
	global_store_dwordx4 v[198:199], v[90:93], off
	v_lshl_add_u64 v[248:249], v[232:233], 2, s[72:73]
	global_load_dwordx4 v[200:203], v[248:249], off offset:528
	global_load_dwordx4 v[204:207], v[248:249], off offset:512
	s_waitcnt vmcnt(9)
	v_pk_fma_f32 v[210:211], v[84:85], v[124:125], v[210:211]
	v_pk_fma_f32 v[88:89], v[88:89], v[128:129], v[214:215]
	v_pk_fma_f32 v[86:87], v[86:87], v[126:127], v[212:213]
	v_pk_fma_f32 v[84:85], v[82:83], v[122:123], v[208:209]
	v_cvt_pk_bf16_f32 v82, v86, v87
	v_cvt_pk_bf16_f32 v83, v88, v89
	v_cvt_pk_bf16_f32 v84, v84, v85
	v_cvt_pk_bf16_f32 v85, v210, v211
	v_lshl_add_u64 v[166:167], v[242:243], 1, s[18:19]
	global_store_dwordx4 v[166:167], v[82:85], off
	v_lshl_add_u64 v[250:251], v[234:235], 2, s[72:73]
	global_load_dwordx4 v[208:211], v[250:251], off offset:528
	global_load_dwordx4 v[212:215], v[250:251], off offset:512
	s_waitcnt vmcnt(9)
	v_pk_fma_f32 v[218:219], v[76:77], v[124:125], v[218:219]
	v_pk_fma_f32 v[80:81], v[80:81], v[128:129], v[222:223]
	v_pk_fma_f32 v[78:79], v[78:79], v[126:127], v[220:221]
	v_pk_fma_f32 v[76:77], v[74:75], v[122:123], v[216:217]
	v_cvt_pk_bf16_f32 v74, v78, v79
	v_cvt_pk_bf16_f32 v75, v80, v81
	v_cvt_pk_bf16_f32 v76, v76, v77
	v_cvt_pk_bf16_f32 v77, v218, v219
	v_lshl_add_u64 v[198:199], v[244:245], 1, s[18:19]
	global_store_dwordx4 v[198:199], v[74:77], off
	v_lshl_add_u64 v[248:249], v[236:237], 2, s[72:73]
	global_load_dwordx4 v[216:219], v[248:249], off offset:528
	global_load_dwordx4 v[220:223], v[248:249], off offset:512
	s_waitcnt vmcnt(9)
	v_pk_fma_f32 v[226:227], v[68:69], v[124:125], v[226:227]
	v_pk_fma_f32 v[72:73], v[72:73], v[128:129], v[230:231]
	v_pk_fma_f32 v[70:71], v[70:71], v[126:127], v[228:229]
	v_pk_fma_f32 v[68:69], v[66:67], v[122:123], v[224:225]
	v_cvt_pk_bf16_f32 v66, v70, v71
	v_cvt_pk_bf16_f32 v67, v72, v73
	v_cvt_pk_bf16_f32 v68, v68, v69
	v_cvt_pk_bf16_f32 v69, v226, v227
	v_lshl_add_u64 v[166:167], v[246:247], 1, s[18:19]
	global_store_dwordx4 v[166:167], v[66:69], off
	v_lshl_add_u64 v[250:251], v[238:239], 2, s[72:73]
	global_load_dwordx4 v[224:227], v[250:251], off offset:528
	global_load_dwordx4 v[228:231], v[250:251], off offset:512
	s_waitcnt vmcnt(9)
	v_pk_fma_f32 v[202:203], v[60:61], v[192:193], v[202:203]
	v_pk_fma_f32 v[64:65], v[64:65], v[196:197], v[206:207]
	v_pk_fma_f32 v[62:63], v[62:63], v[194:195], v[204:205]
	v_pk_fma_f32 v[60:61], v[58:59], v[190:191], v[200:201]
	v_cvt_pk_bf16_f32 v58, v62, v63
	v_cvt_pk_bf16_f32 v59, v64, v65
	v_cvt_pk_bf16_f32 v60, v60, v61
	v_cvt_pk_bf16_f32 v61, v202, v203
	v_lshl_add_u64 v[198:199], v[232:233], 1, s[18:19]
	global_store_dwordx4 v[198:199], v[58:61], off offset:256
	v_lshl_add_u64 v[248:249], v[240:241], 2, s[72:73]
	global_load_dwordx4 v[200:203], v[248:249], off offset:528
	global_load_dwordx4 v[204:207], v[248:249], off offset:512
	s_waitcnt vmcnt(9)
	v_pk_fma_f32 v[210:211], v[52:53], v[192:193], v[210:211]
	v_pk_fma_f32 v[56:57], v[56:57], v[196:197], v[214:215]
	v_pk_fma_f32 v[54:55], v[54:55], v[194:195], v[212:213]
	v_pk_fma_f32 v[52:53], v[50:51], v[190:191], v[208:209]
	v_cvt_pk_bf16_f32 v50, v54, v55
	v_cvt_pk_bf16_f32 v51, v56, v57
	v_cvt_pk_bf16_f32 v52, v52, v53
	v_cvt_pk_bf16_f32 v53, v210, v211
	v_lshl_add_u64 v[166:167], v[234:235], 1, s[18:19]
	global_store_dwordx4 v[166:167], v[50:53], off offset:256
	v_lshl_add_u64 v[250:251], v[242:243], 2, s[72:73]
	global_load_dwordx4 v[208:211], v[250:251], off offset:528
	global_load_dwordx4 v[212:215], v[250:251], off offset:512
	s_waitcnt vmcnt(9)
	v_pk_fma_f32 v[218:219], v[44:45], v[192:193], v[218:219]
	v_pk_fma_f32 v[48:49], v[48:49], v[196:197], v[222:223]
	v_pk_fma_f32 v[46:47], v[46:47], v[194:195], v[220:221]
	v_pk_fma_f32 v[44:45], v[42:43], v[190:191], v[216:217]
	v_cvt_pk_bf16_f32 v42, v46, v47
	v_cvt_pk_bf16_f32 v43, v48, v49
	v_cvt_pk_bf16_f32 v44, v44, v45
	v_cvt_pk_bf16_f32 v45, v218, v219
	v_lshl_add_u64 v[198:199], v[236:237], 1, s[18:19]
	global_store_dwordx4 v[198:199], v[42:45], off offset:256
	v_lshl_add_u64 v[248:249], v[244:245], 2, s[72:73]
	global_load_dwordx4 v[216:219], v[248:249], off offset:528
	global_load_dwordx4 v[220:223], v[248:249], off offset:512
	s_waitcnt vmcnt(9)
	v_pk_fma_f32 v[226:227], v[36:37], v[192:193], v[226:227]
	v_pk_fma_f32 v[40:41], v[40:41], v[196:197], v[230:231]
	v_pk_fma_f32 v[38:39], v[38:39], v[194:195], v[228:229]
	v_pk_fma_f32 v[36:37], v[34:35], v[190:191], v[224:225]
	v_cvt_pk_bf16_f32 v34, v38, v39
	v_cvt_pk_bf16_f32 v35, v40, v41
	v_cvt_pk_bf16_f32 v36, v36, v37
	v_cvt_pk_bf16_f32 v37, v226, v227
	v_lshl_add_u64 v[166:167], v[238:239], 1, s[18:19]
	global_store_dwordx4 v[166:167], v[34:37], off offset:256
	v_lshl_add_u64 v[250:251], v[246:247], 2, s[72:73]
	global_load_dwordx4 v[224:227], v[250:251], off offset:528
	global_load_dwordx4 v[228:231], v[250:251], off offset:512
	s_waitcnt vmcnt(9)
	v_pk_fma_f32 v[32:33], v[32:33], v[192:193], v[202:203]
	v_pk_fma_f32 v[28:29], v[28:29], v[196:197], v[206:207]
	v_pk_fma_f32 v[26:27], v[26:27], v[194:195], v[204:205]
	v_pk_fma_f32 v[30:31], v[30:31], v[190:191], v[200:201]
	v_cvt_pk_bf16_f32 v26, v26, v27
	v_cvt_pk_bf16_f32 v27, v28, v29
	v_cvt_pk_bf16_f32 v28, v30, v31
	v_cvt_pk_bf16_f32 v29, v32, v33
	v_lshl_add_u64 v[198:199], v[240:241], 1, s[18:19]
	global_store_dwordx4 v[198:199], v[26:29], off offset:256
	s_waitcnt vmcnt(7)
	v_pk_fma_f32 v[24:25], v[24:25], v[192:193], v[210:211]
	v_pk_fma_f32 v[20:21], v[20:21], v[196:197], v[214:215]
	v_pk_fma_f32 v[18:19], v[18:19], v[194:195], v[212:213]
	v_pk_fma_f32 v[22:23], v[22:23], v[190:191], v[208:209]
	v_cvt_pk_bf16_f32 v18, v18, v19
	v_cvt_pk_bf16_f32 v19, v20, v21
	v_cvt_pk_bf16_f32 v20, v22, v23
	v_cvt_pk_bf16_f32 v21, v24, v25
	v_lshl_add_u64 v[166:167], v[242:243], 1, s[18:19]
	global_store_dwordx4 v[166:167], v[18:21], off offset:256
	s_waitcnt vmcnt(5)
	v_pk_fma_f32 v[16:17], v[16:17], v[192:193], v[218:219]
	v_pk_fma_f32 v[12:13], v[12:13], v[196:197], v[222:223]
	v_pk_fma_f32 v[10:11], v[10:11], v[194:195], v[220:221]
	v_pk_fma_f32 v[14:15], v[14:15], v[190:191], v[216:217]
	v_cvt_pk_bf16_f32 v10, v10, v11
	v_cvt_pk_bf16_f32 v11, v12, v13
	v_cvt_pk_bf16_f32 v12, v14, v15
	v_cvt_pk_bf16_f32 v13, v16, v17
	v_lshl_add_u64 v[198:199], v[244:245], 1, s[18:19]
	global_store_dwordx4 v[198:199], v[10:13], off offset:256
	s_waitcnt vmcnt(3)
	v_pk_fma_f32 v[8:9], v[8:9], v[192:193], v[226:227]
	v_pk_fma_f32 v[4:5], v[4:5], v[196:197], v[230:231]
	v_pk_fma_f32 v[2:3], v[2:3], v[194:195], v[228:229]
	v_pk_fma_f32 v[6:7], v[6:7], v[190:191], v[224:225]
	v_cvt_pk_bf16_f32 v2, v2, v3
	v_cvt_pk_bf16_f32 v3, v4, v5
	v_cvt_pk_bf16_f32 v4, v6, v7
	v_cvt_pk_bf16_f32 v5, v8, v9
	v_lshl_add_u64 v[166:167], v[246:247], 1, s[18:19]
	global_store_dwordx4 v[166:167], v[2:5], off offset:256
	s_cbranch_vccnz .LBB0_341
	s_andn2_b64 vcc, exec, s[0:1]
	s_cbranch_vccnz .LBB0_340
	s_barrier
	s_branch .LBB0_340
